# speedup vs baseline: 1.0329x; 1.0019x over previous
.LBB0_4:
	s_load_dwordx4 s[20:23], s[0:1], 0x38
	s_load_dwordx2 s[18:19], s[0:1], 0x48
	s_ashr_i32 s2, s2, 3
	s_add_i32 s2, s3, s2
	s_ashr_i32 s33, s2, 3
	s_waitcnt lgkmcnt(0)
	s_mul_i32 s33, s33, s21
	s_mul_i32 s69, s33, s20
	v_bfe_u32 v18, v0, 2, 6
	s_and_b32 s3, s2, 7
	s_mul_i32 s82, s20, s21
	v_cmp_gt_u32_e32 vcc, s82, v18
	s_nop 1
	v_cndmask_b32_e32 v2, 0, v18, vcc
	v_add_u32_e32 v2, s69, v2
	s_add_i32 s2, s22, -1
	v_min_i32_e32 v2, s2, v2
	v_ashrrev_i32_e32 v3, 31, v2
	v_lshlrev_b64 v[6:7], 10, v[2:3]
	v_lshlrev_b32_e32 v2, 4, v0
	v_and_b32_e32 v19, 48, v2
	v_or_b32_e32 v6, v6, v19
	v_lshl_add_u64 v[36:37], s[8:9], 0, v[6:7]
	global_load_dwordx4 v[2:5], v[36:37], off
	v_lshl_add_u64 v[34:35], s[10:11], 0, v[6:7]
	global_load_dwordx4 v[6:9], v[34:35], off
	v_lshrrev_b32_e32 v40, 7, v0
	v_and_b32_e32 v1, 63, v0
	v_bfe_u32 v41, v0, 6, 1
	v_lshlrev_b32_e32 v10, 4, v40
	s_lshl_b32 s2, s3, 1
	v_or3_b32 v10, s2, v10, v41
	v_lshlrev_b32_e32 v11, 3, v1
	s_lshl_b32 s22, s3, 6
	v_and_b32_e32 v42, 31, v0
	v_lshl_or_b32 v14, v10, 14, v11
	v_lshl_or_b32 v10, v40, 9, s22
	v_lshlrev_b32_e32 v11, 5, v41
	v_or3_b32 v10, v10, v11, v42
	v_lshlrev_b32_e32 v15, 2, v10
	global_load_dword v39, v15, s[12:13]
	global_load_dwordx4 v[10:13], v[36:37], off offset:64
	v_lshlrev_b32_e32 v46, 1, v14
	global_load_dwordx4 v[48:51], v46, s[4:5]
	global_load_dwordx4 v[14:17], v[34:35], off offset:64
	global_load_dwordx4 v[52:55], v46, s[6:7]
	global_load_dwordx4 v[56:59], v46, s[4:5] offset:1024
	global_load_dwordx4 v[60:63], v46, s[6:7] offset:1024
	global_load_dwordx4 v[64:67], v46, s[4:5] offset:2048
	global_load_dwordx4 v[68:71], v46, s[6:7] offset:2048
	global_load_dwordx4 v[72:75], v[36:37], off offset:128
	global_load_dwordx4 v[76:79], v[34:35], off offset:128
	v_bfe_u32 v43, v0, 5, 1
	v_mul_u32_u24_e32 v18, 40, v18
	v_mul_u32_u24_e32 v20, 0x50, v42
	v_lshl_add_u32 v44, v18, 1, v19
	v_lshl_add_u32 v45, v43, 4, v20
	v_lshrrev_b32_e32 v38, 6, v0
	s_waitcnt vmcnt(12)
	ds_write_b128 v44, v[2:5]
	s_waitcnt vmcnt(11)
	ds_write_b128 v44, v[6:9] offset:5120
	s_waitcnt lgkmcnt(0)
	s_barrier
	ds_read_b128 v[2:5], v45 offset:5120
	ds_read_b128 v[6:9], v45 offset:7680
	ds_read_b128 v[80:83], v45
	ds_read_b128 v[84:87], v45 offset:2560
	ds_read_b128 v[88:91], v45 offset:5152
	s_waitcnt vmcnt(8) lgkmcnt(4)
	v_mfma_f32_32x32x16_f16 v[18:33], v[2:5], v[48:51], 0
	ds_read_b128 v[92:95], v45 offset:32
	ds_write_b128 v44, v[10:13] offset:10240
	s_waitcnt vmcnt(6) lgkmcnt(4)
	v_mfma_f32_32x32x16_f16 v[18:33], v[80:83], v[52:55], v[18:33]
	ds_read_b128 v[96:99], v45 offset:7712
	v_mfma_f32_32x32x16_f16 v[18:33], v[80:83], v[48:51], v[18:33]
	ds_read_b128 v[80:83], v45 offset:2592
	ds_write_b128 v44, v[14:17] offset:15360
	v_mfma_f32_32x32x16_f16 v[2:17], v[6:9], v[48:51], 0
	global_load_dwordx4 v[100:103], v46, s[4:5] offset:3072
	global_load_dwordx4 v[104:107], v46, s[6:7] offset:3072
	s_waitcnt lgkmcnt(6)
	v_mfma_f32_32x32x16_f16 v[2:17], v[84:87], v[52:55], v[2:17]
	v_mfma_f32_32x32x16_f16 v[2:17], v[84:87], v[48:51], v[2:17]
	s_waitcnt lgkmcnt(0)
	s_barrier
	ds_read_b128 v[48:51], v45 offset:15360
	v_or_b32_e32 v47, 0x1000, v46
	s_waitcnt vmcnt(7)
	v_mfma_f32_32x32x16_f16 v[18:33], v[88:91], v[56:59], v[18:33]
	global_load_dwordx4 v[52:55], v[36:37], off offset:192
	ds_read_b128 v[84:87], v45 offset:10240
	s_waitcnt vmcnt(7)
	v_mfma_f32_32x32x16_f16 v[18:33], v[92:95], v[60:63], v[18:33]
	ds_read_b128 v[88:91], v45 offset:17920
	v_mfma_f32_32x32x16_f16 v[18:33], v[92:95], v[56:59], v[18:33]
	global_load_dwordx4 v[92:95], v[34:35], off offset:192
	ds_read_b128 v[108:111], v45 offset:12800
	v_mfma_f32_32x32x16_f16 v[2:17], v[96:99], v[56:59], v[2:17]
	global_load_dwordx4 v[96:99], v47, s[4:5]
	global_load_dwordx4 v[112:115], v47, s[6:7]
	v_mfma_f32_32x32x16_f16 v[2:17], v[80:83], v[60:63], v[2:17]
	v_mfma_f32_32x32x16_f16 v[2:17], v[80:83], v[56:59], v[2:17]
	ds_read_b128 v[56:59], v45 offset:15392
	v_or_b32_e32 v47, 0x1400, v46
	s_waitcnt vmcnt(9) lgkmcnt(4)
	v_mfma_f32_32x32x16_f16 v[18:33], v[48:51], v[64:67], v[18:33]
	ds_read_b128 v[48:51], v45 offset:10272
	s_waitcnt vmcnt(7)
	ds_write_b128 v44, v[72:75]
	s_waitcnt lgkmcnt(5)
	v_mfma_f32_32x32x16_f16 v[18:33], v[84:87], v[68:71], v[18:33]
	ds_read_b128 v[60:63], v45 offset:17952
	v_mfma_f32_32x32x16_f16 v[18:33], v[84:87], v[64:67], v[18:33]
	ds_read_b128 v[72:75], v45 offset:12832
	s_waitcnt vmcnt(6)
	ds_write_b128 v44, v[76:79] offset:5120
	s_waitcnt lgkmcnt(7)
	v_mfma_f32_32x32x16_f16 v[2:17], v[88:91], v[64:67], v[2:17]
	global_load_dwordx4 v[76:79], v47, s[4:5]
	global_load_dwordx4 v[80:83], v47, s[6:7]
	s_waitcnt lgkmcnt(6)
	v_mfma_f32_32x32x16_f16 v[2:17], v[108:111], v[68:71], v[2:17]
	v_mfma_f32_32x32x16_f16 v[2:17], v[108:111], v[64:67], v[2:17]
	s_waitcnt lgkmcnt(0)
	s_barrier
	ds_read_b128 v[64:67], v45 offset:5120
	v_or_b32_e32 v47, 0x1800, v46
	s_waitcnt vmcnt(7)
	v_mfma_f32_32x32x16_f16 v[18:33], v[56:59], v[100:103], v[18:33]
	global_load_dwordx4 v[56:59], v[36:37], off offset:256
	ds_read_b128 v[68:71], v45
	s_waitcnt vmcnt(7)
	v_mfma_f32_32x32x16_f16 v[18:33], v[48:51], v[104:107], v[18:33]
	ds_read_b128 v[84:87], v45 offset:7680
	v_mfma_f32_32x32x16_f16 v[18:33], v[48:51], v[100:103], v[18:33]
	global_load_dwordx4 v[48:51], v[34:35], off offset:256
	ds_read_b128 v[88:91], v45 offset:2560
	v_mfma_f32_32x32x16_f16 v[2:17], v[60:63], v[100:103], v[2:17]
	global_load_dwordx4 v[60:63], v47, s[4:5]
	global_load_dwordx4 v[108:111], v47, s[6:7]
	v_mfma_f32_32x32x16_f16 v[2:17], v[72:75], v[104:107], v[2:17]
	v_mfma_f32_32x32x16_f16 v[2:17], v[72:75], v[100:103], v[2:17]
	ds_read_b128 v[72:75], v45 offset:5152
	v_or_b32_e32 v47, 0x1c00, v46
	s_waitcnt vmcnt(7) lgkmcnt(4)
	v_mfma_f32_32x32x16_f16 v[18:33], v[64:67], v[96:99], v[18:33]
	ds_read_b128 v[64:67], v45 offset:32
	ds_write_b128 v44, v[52:55] offset:10240
	s_waitcnt vmcnt(6) lgkmcnt(5)
	v_mfma_f32_32x32x16_f16 v[18:33], v[68:71], v[112:115], v[18:33]
	ds_read_b128 v[52:55], v45 offset:7712
	v_mfma_f32_32x32x16_f16 v[18:33], v[68:71], v[96:99], v[18:33]
	ds_read_b128 v[68:71], v45 offset:2592
	ds_write_b128 v44, v[92:95] offset:15360
	s_waitcnt lgkmcnt(7)
	v_mfma_f32_32x32x16_f16 v[2:17], v[84:87], v[96:99], v[2:17]
	global_load_dwordx4 v[84:87], v47, s[4:5]
	global_load_dwordx4 v[92:95], v47, s[6:7]
	s_waitcnt lgkmcnt(6)
	v_mfma_f32_32x32x16_f16 v[2:17], v[88:91], v[112:115], v[2:17]
	v_mfma_f32_32x32x16_f16 v[2:17], v[88:91], v[96:99], v[2:17]
	s_waitcnt lgkmcnt(0)
	s_barrier
	ds_read_b128 v[88:91], v45 offset:15360
	v_or_b32_e32 v47, 0x2000, v46
	s_waitcnt vmcnt(7)
	v_mfma_f32_32x32x16_f16 v[18:33], v[72:75], v[76:79], v[18:33]
	global_load_dwordx4 v[72:75], v[36:37], off offset:320
	ds_read_b128 v[96:99], v45 offset:10240
	s_waitcnt vmcnt(7)
	v_mfma_f32_32x32x16_f16 v[18:33], v[64:67], v[80:83], v[18:33]
	ds_read_b128 v[100:103], v45 offset:17920
	v_mfma_f32_32x32x16_f16 v[18:33], v[64:67], v[76:79], v[18:33]
	global_load_dwordx4 v[64:67], v[34:35], off offset:320
	ds_read_b128 v[104:107], v45 offset:12800
	v_mfma_f32_32x32x16_f16 v[2:17], v[52:55], v[76:79], v[2:17]
	global_load_dwordx4 v[52:55], v47, s[4:5]
	global_load_dwordx4 v[112:115], v47, s[6:7]
	v_mfma_f32_32x32x16_f16 v[2:17], v[68:71], v[80:83], v[2:17]
	v_mfma_f32_32x32x16_f16 v[2:17], v[68:71], v[76:79], v[2:17]
	ds_read_b128 v[68:71], v45 offset:15392
	v_or_b32_e32 v47, 0x2400, v46
	s_waitcnt vmcnt(7) lgkmcnt(4)
	v_mfma_f32_32x32x16_f16 v[18:33], v[88:91], v[60:63], v[18:33]
	ds_read_b128 v[76:79], v45 offset:10272
	ds_write_b128 v44, v[56:59]
	s_waitcnt vmcnt(6) lgkmcnt(5)
	v_mfma_f32_32x32x16_f16 v[18:33], v[96:99], v[108:111], v[18:33]
	ds_read_b128 v[56:59], v45 offset:17952
	v_mfma_f32_32x32x16_f16 v[18:33], v[96:99], v[60:63], v[18:33]
	ds_read_b128 v[80:83], v45 offset:12832
	ds_write_b128 v44, v[48:51] offset:5120
	s_waitcnt lgkmcnt(7)
	v_mfma_f32_32x32x16_f16 v[2:17], v[100:103], v[60:63], v[2:17]
	global_load_dwordx4 v[48:51], v47, s[4:5]
	global_load_dwordx4 v[88:91], v47, s[6:7]
	s_waitcnt lgkmcnt(6)
	v_mfma_f32_32x32x16_f16 v[2:17], v[104:107], v[108:111], v[2:17]
	v_mfma_f32_32x32x16_f16 v[2:17], v[104:107], v[60:63], v[2:17]
	s_waitcnt lgkmcnt(0)
	s_barrier
	ds_read_b128 v[60:63], v45 offset:5120
	v_or_b32_e32 v47, 0x2800, v46
	s_waitcnt vmcnt(7)
	v_mfma_f32_32x32x16_f16 v[18:33], v[68:71], v[84:87], v[18:33]
	global_load_dwordx4 v[68:71], v[36:37], off offset:384
	ds_read_b128 v[96:99], v45
	s_waitcnt vmcnt(7)
	v_mfma_f32_32x32x16_f16 v[18:33], v[76:79], v[92:95], v[18:33]
	ds_read_b128 v[100:103], v45 offset:7680
	v_mfma_f32_32x32x16_f16 v[18:33], v[76:79], v[84:87], v[18:33]
	global_load_dwordx4 v[76:79], v[34:35], off offset:384
	ds_read_b128 v[104:107], v45 offset:2560
	v_mfma_f32_32x32x16_f16 v[2:17], v[56:59], v[84:87], v[2:17]
	global_load_dwordx4 v[56:59], v47, s[4:5]
	global_load_dwordx4 v[108:111], v47, s[6:7]
	v_mfma_f32_32x32x16_f16 v[2:17], v[80:83], v[92:95], v[2:17]
	v_mfma_f32_32x32x16_f16 v[2:17], v[80:83], v[84:87], v[2:17]
	ds_read_b128 v[80:83], v45 offset:5152
	v_or_b32_e32 v47, 0x2c00, v46
	s_waitcnt vmcnt(7) lgkmcnt(4)
	v_mfma_f32_32x32x16_f16 v[18:33], v[60:63], v[52:55], v[18:33]
	ds_read_b128 v[60:63], v45 offset:32
	ds_write_b128 v44, v[72:75] offset:10240
	s_waitcnt vmcnt(6) lgkmcnt(5)
	v_mfma_f32_32x32x16_f16 v[18:33], v[96:99], v[112:115], v[18:33]
	ds_read_b128 v[72:75], v45 offset:7712
	v_mfma_f32_32x32x16_f16 v[18:33], v[96:99], v[52:55], v[18:33]
	ds_read_b128 v[84:87], v45 offset:2592
	ds_write_b128 v44, v[64:67] offset:15360
	s_waitcnt lgkmcnt(7)
	v_mfma_f32_32x32x16_f16 v[2:17], v[100:103], v[52:55], v[2:17]
	global_load_dwordx4 v[64:67], v47, s[4:5]
	global_load_dwordx4 v[92:95], v47, s[6:7]
	s_waitcnt lgkmcnt(6)
	v_mfma_f32_32x32x16_f16 v[2:17], v[104:107], v[112:115], v[2:17]
	v_mfma_f32_32x32x16_f16 v[2:17], v[104:107], v[52:55], v[2:17]
	s_waitcnt lgkmcnt(0)
	s_barrier
	ds_read_b128 v[52:55], v45 offset:15360
	v_or_b32_e32 v47, 0x3000, v46
	s_waitcnt vmcnt(7)
	v_mfma_f32_32x32x16_f16 v[18:33], v[80:83], v[48:51], v[18:33]
	global_load_dwordx4 v[80:83], v[36:37], off offset:448
	ds_read_b128 v[96:99], v45 offset:10240
	s_waitcnt vmcnt(7)
	v_mfma_f32_32x32x16_f16 v[18:33], v[60:63], v[88:91], v[18:33]
	ds_read_b128 v[100:103], v45 offset:17920
	v_mfma_f32_32x32x16_f16 v[18:33], v[60:63], v[48:51], v[18:33]
	global_load_dwordx4 v[60:63], v[34:35], off offset:448
	ds_read_b128 v[104:107], v45 offset:12800
	v_mfma_f32_32x32x16_f16 v[2:17], v[72:75], v[48:51], v[2:17]
	global_load_dwordx4 v[72:75], v47, s[4:5]
	global_load_dwordx4 v[112:115], v47, s[6:7]
	v_mfma_f32_32x32x16_f16 v[2:17], v[84:87], v[88:91], v[2:17]
	v_mfma_f32_32x32x16_f16 v[2:17], v[84:87], v[48:51], v[2:17]
	ds_read_b128 v[48:51], v45 offset:15392
	v_or_b32_e32 v47, 0x3400, v46
	s_waitcnt vmcnt(7) lgkmcnt(4)
	v_mfma_f32_32x32x16_f16 v[18:33], v[52:55], v[56:59], v[18:33]
	ds_read_b128 v[52:55], v45 offset:10272
	ds_write_b128 v44, v[68:71]
	s_waitcnt vmcnt(6) lgkmcnt(5)
	v_mfma_f32_32x32x16_f16 v[18:33], v[96:99], v[108:111], v[18:33]
	ds_read_b128 v[68:71], v45 offset:17952
	v_mfma_f32_32x32x16_f16 v[18:33], v[96:99], v[56:59], v[18:33]
	ds_read_b128 v[84:87], v45 offset:12832
	ds_write_b128 v44, v[76:79] offset:5120
	s_waitcnt lgkmcnt(7)
	v_mfma_f32_32x32x16_f16 v[2:17], v[100:103], v[56:59], v[2:17]
	global_load_dwordx4 v[76:79], v47, s[4:5]
	global_load_dwordx4 v[88:91], v47, s[6:7]
	s_waitcnt lgkmcnt(6)
	v_mfma_f32_32x32x16_f16 v[2:17], v[104:107], v[108:111], v[2:17]
	v_mfma_f32_32x32x16_f16 v[2:17], v[104:107], v[56:59], v[2:17]
	s_waitcnt lgkmcnt(0)
	s_barrier
	ds_read_b128 v[56:59], v45 offset:5120
	v_or_b32_e32 v47, 0x3800, v46
	s_waitcnt vmcnt(7)
	v_mfma_f32_32x32x16_f16 v[18:33], v[48:51], v[64:67], v[18:33]
	global_load_dwordx4 v[48:51], v[36:37], off offset:512
	ds_read_b128 v[96:99], v45
	s_waitcnt vmcnt(7)
	v_mfma_f32_32x32x16_f16 v[18:33], v[52:55], v[92:95], v[18:33]
	ds_read_b128 v[100:103], v45 offset:7680
	v_mfma_f32_32x32x16_f16 v[18:33], v[52:55], v[64:67], v[18:33]
	global_load_dwordx4 v[52:55], v[34:35], off offset:512
	ds_read_b128 v[104:107], v45 offset:2560
	v_mfma_f32_32x32x16_f16 v[2:17], v[68:71], v[64:67], v[2:17]
	global_load_dwordx4 v[68:71], v47, s[4:5]
	global_load_dwordx4 v[108:111], v47, s[6:7]
	v_mfma_f32_32x32x16_f16 v[2:17], v[84:87], v[92:95], v[2:17]
	v_mfma_f32_32x32x16_f16 v[2:17], v[84:87], v[64:67], v[2:17]
	ds_read_b128 v[64:67], v45 offset:5152
	v_or_b32_e32 v47, 0x3c00, v46
	s_waitcnt vmcnt(7) lgkmcnt(4)
	v_mfma_f32_32x32x16_f16 v[18:33], v[56:59], v[72:75], v[18:33]
	ds_read_b128 v[56:59], v45 offset:32
	ds_write_b128 v44, v[80:83] offset:10240
	s_waitcnt vmcnt(6) lgkmcnt(5)
	v_mfma_f32_32x32x16_f16 v[18:33], v[96:99], v[112:115], v[18:33]
	ds_read_b128 v[80:83], v45 offset:7712
	v_mfma_f32_32x32x16_f16 v[18:33], v[96:99], v[72:75], v[18:33]
	ds_read_b128 v[84:87], v45 offset:2592
	ds_write_b128 v44, v[60:63] offset:15360
	s_waitcnt lgkmcnt(7)
	v_mfma_f32_32x32x16_f16 v[2:17], v[100:103], v[72:75], v[2:17]
	global_load_dwordx4 v[60:63], v47, s[4:5]
	global_load_dwordx4 v[92:95], v47, s[6:7]
	s_waitcnt lgkmcnt(6)
	v_mfma_f32_32x32x16_f16 v[2:17], v[104:107], v[112:115], v[2:17]
	v_mfma_f32_32x32x16_f16 v[2:17], v[104:107], v[72:75], v[2:17]
	s_waitcnt lgkmcnt(0)
	s_barrier
	ds_read_b128 v[72:75], v45 offset:15360
	v_or_b32_e32 v47, 0x4000, v46
	s_waitcnt vmcnt(7)
	v_mfma_f32_32x32x16_f16 v[18:33], v[64:67], v[76:79], v[18:33]
	global_load_dwordx4 v[64:67], v[36:37], off offset:576
	ds_read_b128 v[96:99], v45 offset:10240
	s_waitcnt vmcnt(7)
	v_mfma_f32_32x32x16_f16 v[18:33], v[56:59], v[88:91], v[18:33]
	ds_read_b128 v[100:103], v45 offset:17920
	v_mfma_f32_32x32x16_f16 v[18:33], v[56:59], v[76:79], v[18:33]
	global_load_dwordx4 v[56:59], v[34:35], off offset:576
	ds_read_b128 v[104:107], v45 offset:12800
	v_mfma_f32_32x32x16_f16 v[2:17], v[80:83], v[76:79], v[2:17]
	global_load_dwordx4 v[80:83], v47, s[4:5]
	global_load_dwordx4 v[112:115], v47, s[6:7]
	v_mfma_f32_32x32x16_f16 v[2:17], v[84:87], v[88:91], v[2:17]
	v_mfma_f32_32x32x16_f16 v[2:17], v[84:87], v[76:79], v[2:17]
	ds_read_b128 v[76:79], v45 offset:15392
	s_movk_i32 s66, 0x4400
	v_or_b32_e32 v47, 0x4400, v46
	s_waitcnt vmcnt(7) lgkmcnt(4)
	v_mfma_f32_32x32x16_f16 v[18:33], v[72:75], v[68:71], v[18:33]
	ds_read_b128 v[72:75], v45 offset:10272
	ds_write_b128 v44, v[48:51]
	s_waitcnt vmcnt(6) lgkmcnt(5)
	v_mfma_f32_32x32x16_f16 v[18:33], v[96:99], v[108:111], v[18:33]
	ds_read_b128 v[48:51], v45 offset:17952
	v_mfma_f32_32x32x16_f16 v[18:33], v[96:99], v[68:71], v[18:33]
	ds_read_b128 v[84:87], v45 offset:12832
	ds_write_b128 v44, v[52:55] offset:5120
	s_waitcnt lgkmcnt(7)
	v_mfma_f32_32x32x16_f16 v[2:17], v[100:103], v[68:71], v[2:17]
	global_load_dwordx4 v[52:55], v47, s[4:5]
	global_load_dwordx4 v[88:91], v47, s[6:7]
	s_waitcnt lgkmcnt(6)
	v_mfma_f32_32x32x16_f16 v[2:17], v[104:107], v[108:111], v[2:17]
	v_mfma_f32_32x32x16_f16 v[2:17], v[104:107], v[68:71], v[2:17]
	s_waitcnt lgkmcnt(0)
	s_barrier
	ds_read_b128 v[68:71], v45 offset:5120
	v_or_b32_e32 v47, 0x4800, v46
	s_waitcnt vmcnt(7)
	v_mfma_f32_32x32x16_f16 v[18:33], v[76:79], v[60:63], v[18:33]
	global_load_dwordx4 v[76:79], v[36:37], off offset:640
	ds_read_b128 v[96:99], v45
	s_waitcnt vmcnt(7)
	v_mfma_f32_32x32x16_f16 v[18:33], v[72:75], v[92:95], v[18:33]
	ds_read_b128 v[100:103], v45 offset:7680
	v_mfma_f32_32x32x16_f16 v[18:33], v[72:75], v[60:63], v[18:33]
	global_load_dwordx4 v[72:75], v[34:35], off offset:640
	ds_read_b128 v[104:107], v45 offset:2560
	v_mfma_f32_32x32x16_f16 v[2:17], v[48:51], v[60:63], v[2:17]
	global_load_dwordx4 v[48:51], v47, s[4:5]
	global_load_dwordx4 v[108:111], v47, s[6:7]
	v_mfma_f32_32x32x16_f16 v[2:17], v[84:87], v[92:95], v[2:17]
	v_mfma_f32_32x32x16_f16 v[2:17], v[84:87], v[60:63], v[2:17]
	ds_read_b128 v[60:63], v45 offset:5152
	v_or_b32_e32 v47, 0x4c00, v46
	s_waitcnt vmcnt(7) lgkmcnt(4)
	v_mfma_f32_32x32x16_f16 v[18:33], v[68:71], v[80:83], v[18:33]
	ds_read_b128 v[68:71], v45 offset:32
	ds_write_b128 v44, v[64:67] offset:10240
	s_waitcnt vmcnt(6) lgkmcnt(5)
	v_mfma_f32_32x32x16_f16 v[18:33], v[96:99], v[112:115], v[18:33]
	ds_read_b128 v[64:67], v45 offset:7712
	v_mfma_f32_32x32x16_f16 v[18:33], v[96:99], v[80:83], v[18:33]
	ds_read_b128 v[84:87], v45 offset:2592
	ds_write_b128 v44, v[56:59] offset:15360
	s_waitcnt lgkmcnt(7)
	v_mfma_f32_32x32x16_f16 v[2:17], v[100:103], v[80:83], v[2:17]
	global_load_dwordx4 v[56:59], v47, s[4:5]
	global_load_dwordx4 v[92:95], v47, s[6:7]
	s_waitcnt lgkmcnt(6)
	v_mfma_f32_32x32x16_f16 v[2:17], v[104:107], v[112:115], v[2:17]
	v_mfma_f32_32x32x16_f16 v[2:17], v[104:107], v[80:83], v[2:17]
	s_waitcnt lgkmcnt(0)
	s_barrier
	ds_read_b128 v[80:83], v45 offset:15360
	v_or_b32_e32 v47, 0x5000, v46
	s_waitcnt vmcnt(7)
	v_mfma_f32_32x32x16_f16 v[18:33], v[60:63], v[52:55], v[18:33]
	global_load_dwordx4 v[60:63], v[36:37], off offset:704
	ds_read_b128 v[96:99], v45 offset:10240
	s_waitcnt vmcnt(7)
	v_mfma_f32_32x32x16_f16 v[18:33], v[68:71], v[88:91], v[18:33]
	ds_read_b128 v[100:103], v45 offset:17920
	v_mfma_f32_32x32x16_f16 v[18:33], v[68:71], v[52:55], v[18:33]
	global_load_dwordx4 v[68:71], v[34:35], off offset:704
	ds_read_b128 v[104:107], v45 offset:12800
	v_mfma_f32_32x32x16_f16 v[2:17], v[64:67], v[52:55], v[2:17]
	global_load_dwordx4 v[64:67], v47, s[4:5]
	global_load_dwordx4 v[112:115], v47, s[6:7]
	v_mfma_f32_32x32x16_f16 v[2:17], v[84:87], v[88:91], v[2:17]
	v_mfma_f32_32x32x16_f16 v[2:17], v[84:87], v[52:55], v[2:17]
	ds_read_b128 v[52:55], v45 offset:15392
	v_or_b32_e32 v47, 0x5400, v46
	s_waitcnt vmcnt(7) lgkmcnt(4)
	v_mfma_f32_32x32x16_f16 v[18:33], v[80:83], v[48:51], v[18:33]
	ds_read_b128 v[80:83], v45 offset:10272
	ds_write_b128 v44, v[76:79]
	s_waitcnt vmcnt(6) lgkmcnt(5)
	v_mfma_f32_32x32x16_f16 v[18:33], v[96:99], v[108:111], v[18:33]
	ds_read_b128 v[76:79], v45 offset:17952
	v_mfma_f32_32x32x16_f16 v[18:33], v[96:99], v[48:51], v[18:33]
	ds_read_b128 v[84:87], v45 offset:12832
	ds_write_b128 v44, v[72:75] offset:5120
	s_waitcnt lgkmcnt(7)
	v_mfma_f32_32x32x16_f16 v[2:17], v[100:103], v[48:51], v[2:17]
	global_load_dwordx4 v[72:75], v47, s[4:5]
	global_load_dwordx4 v[88:91], v47, s[6:7]
	s_waitcnt lgkmcnt(6)
	v_mfma_f32_32x32x16_f16 v[2:17], v[104:107], v[108:111], v[2:17]
	v_mfma_f32_32x32x16_f16 v[2:17], v[104:107], v[48:51], v[2:17]
	s_waitcnt lgkmcnt(0)
	s_barrier
	ds_read_b128 v[48:51], v45 offset:5120
	v_or_b32_e32 v47, 0x5800, v46
	s_waitcnt vmcnt(7)
	v_mfma_f32_32x32x16_f16 v[18:33], v[52:55], v[56:59], v[18:33]
	global_load_dwordx4 v[52:55], v[36:37], off offset:768
	ds_read_b128 v[96:99], v45
	s_waitcnt vmcnt(7)
	v_mfma_f32_32x32x16_f16 v[18:33], v[80:83], v[92:95], v[18:33]
	ds_read_b128 v[100:103], v45 offset:7680
	v_mfma_f32_32x32x16_f16 v[18:33], v[80:83], v[56:59], v[18:33]
	global_load_dwordx4 v[80:83], v[34:35], off offset:768
	ds_read_b128 v[104:107], v45 offset:2560
	v_mfma_f32_32x32x16_f16 v[2:17], v[76:79], v[56:59], v[2:17]
	global_load_dwordx4 v[76:79], v47, s[4:5]
	global_load_dwordx4 v[108:111], v47, s[6:7]
	v_mfma_f32_32x32x16_f16 v[2:17], v[84:87], v[92:95], v[2:17]
	v_mfma_f32_32x32x16_f16 v[2:17], v[84:87], v[56:59], v[2:17]
	ds_read_b128 v[56:59], v45 offset:5152
	v_or_b32_e32 v47, 0x5c00, v46
	s_waitcnt vmcnt(7) lgkmcnt(4)
	v_mfma_f32_32x32x16_f16 v[18:33], v[48:51], v[64:67], v[18:33]
	ds_read_b128 v[48:51], v45 offset:32
	ds_write_b128 v44, v[60:63] offset:10240
	s_waitcnt vmcnt(6) lgkmcnt(5)
	v_mfma_f32_32x32x16_f16 v[18:33], v[96:99], v[112:115], v[18:33]
	ds_read_b128 v[60:63], v45 offset:7712
	v_mfma_f32_32x32x16_f16 v[18:33], v[96:99], v[64:67], v[18:33]
	ds_read_b128 v[84:87], v45 offset:2592
	ds_write_b128 v44, v[68:71] offset:15360
	s_waitcnt lgkmcnt(7)
	v_mfma_f32_32x32x16_f16 v[2:17], v[100:103], v[64:67], v[2:17]
	global_load_dwordx4 v[68:71], v47, s[4:5]
	global_load_dwordx4 v[92:95], v47, s[6:7]
	s_waitcnt lgkmcnt(6)
	v_mfma_f32_32x32x16_f16 v[2:17], v[104:107], v[112:115], v[2:17]
	v_mfma_f32_32x32x16_f16 v[2:17], v[104:107], v[64:67], v[2:17]
	s_waitcnt lgkmcnt(0)
	s_barrier
	ds_read_b128 v[64:67], v45 offset:15360
	v_or_b32_e32 v47, 0x6000, v46
	s_waitcnt vmcnt(7)
	v_mfma_f32_32x32x16_f16 v[18:33], v[56:59], v[72:75], v[18:33]
	global_load_dwordx4 v[56:59], v[36:37], off offset:832
	ds_read_b128 v[96:99], v45 offset:10240
	s_waitcnt vmcnt(7)
	v_mfma_f32_32x32x16_f16 v[18:33], v[48:51], v[88:91], v[18:33]
	ds_read_b128 v[100:103], v45 offset:17920
	v_mfma_f32_32x32x16_f16 v[18:33], v[48:51], v[72:75], v[18:33]
	global_load_dwordx4 v[48:51], v[34:35], off offset:832
	ds_read_b128 v[104:107], v45 offset:12800
	v_mfma_f32_32x32x16_f16 v[2:17], v[60:63], v[72:75], v[2:17]
	global_load_dwordx4 v[60:63], v47, s[4:5]
	global_load_dwordx4 v[112:115], v47, s[6:7]
	v_mfma_f32_32x32x16_f16 v[2:17], v[84:87], v[88:91], v[2:17]
	v_mfma_f32_32x32x16_f16 v[2:17], v[84:87], v[72:75], v[2:17]
	ds_read_b128 v[72:75], v45 offset:15392
	v_or_b32_e32 v47, 0x6400, v46
	s_waitcnt vmcnt(7) lgkmcnt(4)
	v_mfma_f32_32x32x16_f16 v[18:33], v[64:67], v[76:79], v[18:33]
	ds_read_b128 v[64:67], v45 offset:10272
	ds_write_b128 v44, v[52:55]
	s_waitcnt vmcnt(6) lgkmcnt(5)
	v_mfma_f32_32x32x16_f16 v[18:33], v[96:99], v[108:111], v[18:33]
	ds_read_b128 v[52:55], v45 offset:17952
	v_mfma_f32_32x32x16_f16 v[18:33], v[96:99], v[76:79], v[18:33]
	ds_read_b128 v[84:87], v45 offset:12832
	ds_write_b128 v44, v[80:83] offset:5120
	s_waitcnt lgkmcnt(7)
	v_mfma_f32_32x32x16_f16 v[2:17], v[100:103], v[76:79], v[2:17]
	global_load_dwordx4 v[80:83], v47, s[4:5]
	global_load_dwordx4 v[88:91], v47, s[6:7]
	s_waitcnt lgkmcnt(6)
	v_mfma_f32_32x32x16_f16 v[2:17], v[104:107], v[108:111], v[2:17]
	v_mfma_f32_32x32x16_f16 v[2:17], v[104:107], v[76:79], v[2:17]
	s_waitcnt lgkmcnt(0)
	s_barrier
	ds_read_b128 v[76:79], v45 offset:5120
	v_or_b32_e32 v47, 0x6800, v46
	s_waitcnt vmcnt(7)
	v_mfma_f32_32x32x16_f16 v[18:33], v[72:75], v[68:71], v[18:33]
	global_load_dwordx4 v[72:75], v[36:37], off offset:896
	ds_read_b128 v[96:99], v45
	s_waitcnt vmcnt(7)
	v_mfma_f32_32x32x16_f16 v[18:33], v[64:67], v[92:95], v[18:33]
	ds_read_b128 v[100:103], v45 offset:7680
	v_mfma_f32_32x32x16_f16 v[18:33], v[64:67], v[68:71], v[18:33]
	global_load_dwordx4 v[64:67], v[34:35], off offset:896
	ds_read_b128 v[104:107], v45 offset:2560
	v_mfma_f32_32x32x16_f16 v[2:17], v[52:55], v[68:71], v[2:17]
	global_load_dwordx4 v[52:55], v47, s[4:5]
	global_load_dwordx4 v[108:111], v47, s[6:7]
	v_mfma_f32_32x32x16_f16 v[2:17], v[84:87], v[92:95], v[2:17]
	v_mfma_f32_32x32x16_f16 v[2:17], v[84:87], v[68:71], v[2:17]
	ds_read_b128 v[68:71], v45 offset:5152
	v_or_b32_e32 v47, 0x6c00, v46
	s_waitcnt vmcnt(7) lgkmcnt(4)
	v_mfma_f32_32x32x16_f16 v[18:33], v[76:79], v[60:63], v[18:33]
	ds_read_b128 v[76:79], v45 offset:32
	ds_write_b128 v44, v[56:59] offset:10240
	s_waitcnt vmcnt(6) lgkmcnt(5)
	v_mfma_f32_32x32x16_f16 v[18:33], v[96:99], v[112:115], v[18:33]
	ds_read_b128 v[56:59], v45 offset:7712
	v_mfma_f32_32x32x16_f16 v[18:33], v[96:99], v[60:63], v[18:33]
	ds_read_b128 v[84:87], v45 offset:2592
	ds_write_b128 v44, v[48:51] offset:15360
	s_waitcnt lgkmcnt(7)
	v_mfma_f32_32x32x16_f16 v[2:17], v[100:103], v[60:63], v[2:17]
	global_load_dwordx4 v[48:51], v47, s[4:5]
	global_load_dwordx4 v[92:95], v47, s[6:7]
	s_waitcnt lgkmcnt(6)
	v_mfma_f32_32x32x16_f16 v[2:17], v[104:107], v[112:115], v[2:17]
	v_mfma_f32_32x32x16_f16 v[2:17], v[104:107], v[60:63], v[2:17]
	s_waitcnt lgkmcnt(0)
	s_barrier
	ds_read_b128 v[60:63], v45 offset:15360
	v_or_b32_e32 v47, 0x7000, v46
	s_waitcnt vmcnt(7)
	v_mfma_f32_32x32x16_f16 v[18:33], v[68:71], v[80:83], v[18:33]
	global_load_dwordx4 v[68:71], v[36:37], off offset:960
	ds_read_b128 v[96:99], v45 offset:10240
	s_waitcnt vmcnt(7)
	v_mfma_f32_32x32x16_f16 v[18:33], v[76:79], v[88:91], v[18:33]
	ds_read_b128 v[100:103], v45 offset:17920
	v_mfma_f32_32x32x16_f16 v[18:33], v[76:79], v[80:83], v[18:33]
	global_load_dwordx4 v[34:37], v[34:35], off offset:960
	ds_read_b128 v[76:79], v45 offset:12800
	v_mfma_f32_32x32x16_f16 v[2:17], v[56:59], v[80:83], v[2:17]
	global_load_dwordx4 v[56:59], v47, s[4:5]
	global_load_dwordx4 v[104:107], v47, s[6:7]
	v_mfma_f32_32x32x16_f16 v[2:17], v[84:87], v[88:91], v[2:17]
	v_mfma_f32_32x32x16_f16 v[2:17], v[84:87], v[80:83], v[2:17]
	ds_read_b128 v[80:83], v45 offset:15392
	v_or_b32_e32 v47, 0x7400, v46
	s_waitcnt vmcnt(7) lgkmcnt(4)
	v_mfma_f32_32x32x16_f16 v[18:33], v[60:63], v[52:55], v[18:33]
	ds_read_b128 v[60:63], v45 offset:10272
	ds_write_b128 v44, v[72:75]
	s_waitcnt vmcnt(6) lgkmcnt(5)
	v_mfma_f32_32x32x16_f16 v[18:33], v[96:99], v[108:111], v[18:33]
	ds_read_b128 v[72:75], v45 offset:17952
	v_mfma_f32_32x32x16_f16 v[18:33], v[96:99], v[52:55], v[18:33]
	ds_read_b128 v[84:87], v45 offset:12832
	ds_write_b128 v44, v[64:67] offset:5120
	s_waitcnt lgkmcnt(7)
	v_mfma_f32_32x32x16_f16 v[2:17], v[100:103], v[52:55], v[2:17]
	global_load_dwordx4 v[64:67], v47, s[4:5]
	global_load_dwordx4 v[88:91], v47, s[6:7]
	s_waitcnt lgkmcnt(6)
	v_mfma_f32_32x32x16_f16 v[2:17], v[76:79], v[108:111], v[2:17]
	v_mfma_f32_32x32x16_f16 v[2:17], v[76:79], v[52:55], v[2:17]
	s_waitcnt lgkmcnt(0)
	s_barrier
	ds_read_b128 v[52:55], v45 offset:5120
	v_or_b32_e32 v47, 0x7800, v46
	s_waitcnt vmcnt(7)
	v_mfma_f32_32x32x16_f16 v[18:33], v[80:83], v[48:51], v[18:33]
	ds_read_b128 v[76:79], v45
	s_waitcnt vmcnt(6)
	v_mfma_f32_32x32x16_f16 v[18:33], v[60:63], v[92:95], v[18:33]
	ds_read_b128 v[80:83], v45 offset:7680
	v_mfma_f32_32x32x16_f16 v[18:33], v[60:63], v[48:51], v[18:33]
	ds_read_b128 v[60:63], v45 offset:2560
	v_mfma_f32_32x32x16_f16 v[2:17], v[72:75], v[48:51], v[2:17]
	global_load_dwordx4 v[72:75], v47, s[4:5]
	global_load_dwordx4 v[96:99], v47, s[6:7]
	v_mfma_f32_32x32x16_f16 v[2:17], v[84:87], v[92:95], v[2:17]
	v_mfma_f32_32x32x16_f16 v[2:17], v[84:87], v[48:51], v[2:17]
	v_or_b32_e32 v100, 0x7c00, v46
	ds_read_b128 v[46:49], v45 offset:5152
	s_waitcnt vmcnt(5) lgkmcnt(4)
	v_mfma_f32_32x32x16_f16 v[18:33], v[52:55], v[56:59], v[18:33]
	ds_read_b128 v[50:53], v45 offset:32
	ds_write_b128 v44, v[68:71] offset:10240
	s_waitcnt vmcnt(4) lgkmcnt(5)
	v_mfma_f32_32x32x16_f16 v[18:33], v[76:79], v[104:107], v[18:33]
	ds_read_b128 v[84:87], v45 offset:7712
	v_mfma_f32_32x32x16_f16 v[18:33], v[76:79], v[56:59], v[18:33]
	ds_read_b128 v[76:79], v45 offset:2592
	ds_write_b128 v44, v[34:37] offset:15360
	s_waitcnt lgkmcnt(7)
	v_mfma_f32_32x32x16_f16 v[2:17], v[80:83], v[56:59], v[2:17]
	global_load_dwordx4 v[80:83], v100, s[4:5]
	global_load_dwordx4 v[92:95], v100, s[6:7]
	s_waitcnt lgkmcnt(6)
	v_mfma_f32_32x32x16_f16 v[2:17], v[60:63], v[104:107], v[2:17]
	v_mfma_f32_32x32x16_f16 v[2:17], v[60:63], v[56:59], v[2:17]
	s_waitcnt lgkmcnt(0)
	s_barrier
	ds_read_b128 v[54:57], v45 offset:15360
	s_waitcnt vmcnt(5)
	v_mfma_f32_32x32x16_f16 v[18:33], v[46:49], v[64:67], v[18:33]
	ds_read_b128 v[46:49], v45 offset:10240
	s_waitcnt vmcnt(4)
	v_mfma_f32_32x32x16_f16 v[18:33], v[50:53], v[88:91], v[18:33]
	ds_read_b128 v[58:61], v45 offset:17920
	v_mfma_f32_32x32x16_f16 v[18:33], v[50:53], v[64:67], v[18:33]
	ds_read_b128 v[50:53], v45 offset:12800
	v_mfma_f32_32x32x16_f16 v[2:17], v[84:87], v[64:67], v[2:17]
	v_mfma_f32_32x32x16_f16 v[2:17], v[76:79], v[88:91], v[2:17]
	v_mfma_f32_32x32x16_f16 v[2:17], v[76:79], v[64:67], v[2:17]
	ds_read_b128 v[62:65], v45 offset:15392
	s_waitcnt vmcnt(3) lgkmcnt(4)
	v_mfma_f32_32x32x16_f16 v[18:33], v[54:57], v[72:75], v[18:33]
	ds_read_b128 v[54:57], v45 offset:10272
	ds_write_b128 v44, v[68:71]
	s_waitcnt vmcnt(2) lgkmcnt(5)
	v_mfma_f32_32x32x16_f16 v[18:33], v[46:49], v[96:99], v[18:33]
	ds_read_b128 v[66:69], v45 offset:17952
	v_mfma_f32_32x32x16_f16 v[18:33], v[46:49], v[72:75], v[18:33]
	ds_read_b128 v[46:49], v45 offset:12832
	ds_write_b128 v44, v[34:37] offset:5120
	s_waitcnt lgkmcnt(7)
	v_mfma_f32_32x32x16_f16 v[2:17], v[58:61], v[72:75], v[2:17]
	s_waitcnt lgkmcnt(6)
	v_mfma_f32_32x32x16_f16 v[2:17], v[50:53], v[96:99], v[2:17]
	v_mfma_f32_32x32x16_f16 v[2:17], v[50:53], v[72:75], v[2:17]
	s_waitcnt lgkmcnt(0)
	s_barrier
	s_waitcnt vmcnt(1)
	v_mfma_f32_32x32x16_f16 v[18:33], v[62:65], v[80:83], v[18:33]
	s_waitcnt vmcnt(0)
	v_mfma_f32_32x32x16_f16 v[18:33], v[54:57], v[92:95], v[18:33]
	v_mfma_f32_32x32x16_f16 v[18:33], v[54:57], v[80:83], v[18:33]
	v_mfma_f32_32x32x16_f16 v[2:17], v[66:69], v[80:83], v[2:17]
	v_mfma_f32_32x32x16_f16 v[2:17], v[46:49], v[92:95], v[2:17]
	v_mfma_f32_32x32x16_f16 v[2:17], v[46:49], v[80:83], v[2:17]
	v_mul_u32_u24_e32 v34, 0x4400, v40
	v_lshlrev_b32_e32 v35, 7, v41
	v_lshlrev_b32_e32 v36, 2, v42
	v_or3_b32 v34, v34, v35, v36
	s_movk_i32 s2, 0x440
	s_nop 3
	v_fma_f32 v18, s19, v18, v39
	v_mad_u32_u24 v34, v43, s2, v34
	v_fma_f32 v19, s19, v19, v39
	s_barrier
	ds_write2_b32 v34, v18, v19 offset1:68
	v_fma_f32 v18, s19, v20, v39
	v_fma_f32 v19, s19, v21, v39
	ds_write2_b32 v34, v18, v19 offset0:136 offset1:204
	v_fma_f32 v18, s19, v22, v39
	v_fma_f32 v19, s19, v23, v39
	v_add_u32_e32 v20, 0x800, v34
	ds_write2_b32 v20, v18, v19 offset0:32 offset1:100
	v_fma_f32 v18, s19, v24, v39
	v_fma_f32 v19, s19, v25, v39
	ds_write2_b32 v20, v18, v19 offset0:168 offset1:236
	v_fma_f32 v18, s19, v26, v39
	v_fma_f32 v19, s19, v27, v39
	v_add_u32_e32 v20, 0x1000, v34
	ds_write2_b32 v20, v18, v19 offset0:64 offset1:132
	v_fma_f32 v18, s19, v28, v39
	v_fma_f32 v19, s19, v29, v39
	v_add_u32_e32 v20, 0x1200, v34
	ds_write2_b32 v20, v18, v19 offset0:72 offset1:140
	v_fma_f32 v18, s19, v30, v39
	v_fma_f32 v19, s19, v31, v39
	v_add_u32_e32 v20, 0x1800, v34
	ds_write2_b32 v20, v18, v19 offset0:96 offset1:164
	v_fma_f32 v18, s19, v32, v39
	v_fma_f32 v19, s19, v33, v39
	v_add_u32_e32 v20, 0x1a00, v34
	ds_write2_b32 v20, v18, v19 offset0:104 offset1:172
	v_fma_f32 v2, s19, v2, v39
	v_fma_f32 v3, s19, v3, v39
	v_add_u32_e32 v18, 0x2000, v34
	ds_write2_b32 v18, v2, v3 offset0:128 offset1:196
	v_fma_f32 v2, s19, v4, v39
	v_fma_f32 v3, s19, v5, v39
	v_add_u32_e32 v4, 0x2400, v34
	ds_write2_b32 v4, v2, v3 offset0:8 offset1:76
	v_fma_f32 v2, s19, v6, v39
	v_fma_f32 v3, s19, v7, v39
	v_add_u32_e32 v4, 0x2800, v34
	ds_write2_b32 v4, v2, v3 offset0:160 offset1:228
	v_fma_f32 v2, s19, v8, v39
	v_fma_f32 v3, s19, v9, v39
	v_add_u32_e32 v4, 0x2c00, v34
	ds_write2_b32 v4, v2, v3 offset0:40 offset1:108
	v_fma_f32 v2, s19, v10, v39
	v_fma_f32 v3, s19, v11, v39
	v_add_u32_e32 v4, 0x3200, v34
	ds_write2_b32 v4, v2, v3 offset0:64 offset1:132
	v_fma_f32 v2, s19, v12, v39
	v_fma_f32 v3, s19, v13, v39
	v_add_u32_e32 v4, 0x3400, v34
	s_sub_i32 s2, 0x100, s33
	ds_write2_b32 v4, v2, v3 offset0:72 offset1:140
	v_fma_f32 v2, s19, v14, v39
	v_fma_f32 v3, s19, v15, v39
	v_add_u32_e32 v4, 0x3a00, v34
	s_min_i32 s21, s21, s2
	ds_write2_b32 v4, v2, v3 offset0:96 offset1:164
	v_fma_f32 v2, s19, v16, v39
	v_fmac_f32_e32 v39, s19, v17
	v_add_u32_e32 v3, 0x3c00, v34
	v_cmp_gt_i32_e32 vcc, s21, v38
	ds_write2_b32 v3, v2, v39 offset0:104 offset1:172
	s_waitcnt lgkmcnt(0)
	s_barrier
	s_and_saveexec_b64 s[2:3], vcc
	s_cbranch_execz .LBB0_59
	v_lshlrev_b32_e32 v2, 2, v0
	v_and_b32_e32 v2, 12, v2
	v_or_b32_e32 v4, 1, v2
	v_lshrrev_b32_e32 v6, 2, v1
	v_cmp_gt_i32_e64 s[6:7], s20, v4
	v_or_b32_e32 v4, 2, v2
	s_load_dwordx4 s[24:27], s[0:1], 0x28
	v_cmp_gt_i32_e32 vcc, s20, v6
	v_cmp_le_i32_e64 s[0:1], s23, v6
	v_cmp_gt_i32_e64 s[10:11], s20, v4
	v_or_b32_e32 v4, 3, v2
	s_and_b64 s[0:1], vcc, s[0:1]
	v_cmp_gt_i32_e64 s[2:3], s20, v2
	v_cmp_gt_i32_e64 s[14:15], s20, v4
	s_and_b64 s[4:5], s[2:3], s[0:1]
	s_and_b64 s[8:9], s[0:1], s[6:7]
	s_and_b64 s[12:13], s[0:1], s[10:11]
	s_and_b64 s[16:17], s[0:1], s[14:15]
	s_cmp_gt_i32 s20, 0
	s_cselect_b64 s[28:29], -1, 0
	s_cmp_eq_u32 s18, 0
	s_cselect_b64 s[18:19], -1, 0
	s_cmp_lt_i32 s23, 1
	s_cselect_b64 s[30:31], -1, 0
	s_and_b64 s[30:31], s[30:31], s[28:29]
	s_cmp_lt_i32 s23, 2
	s_cselect_b64 s[34:35], -1, 0
	s_cmp_gt_i32 s20, 1
	s_cselect_b64 s[36:37], -1, 0
	s_and_b64 s[34:35], s[34:35], s[36:37]
	s_cmp_lt_i32 s23, 3
	s_cselect_b64 s[36:37], -1, 0
	s_cmp_gt_i32 s20, 2
	s_cselect_b64 s[38:39], -1, 0
	s_and_b64 s[36:37], s[36:37], s[38:39]
	s_cmp_lt_i32 s23, 4
	s_cselect_b64 s[38:39], -1, 0
	s_cmp_gt_i32 s20, 3
	s_cselect_b64 s[40:41], -1, 0
	s_and_b64 s[38:39], s[38:39], s[40:41]
	s_cmp_lt_i32 s23, 5
	s_cselect_b64 s[40:41], -1, 0
	s_cmp_gt_i32 s20, 4
	s_cselect_b64 s[42:43], -1, 0
	s_and_b64 s[40:41], s[40:41], s[42:43]
	s_cmp_lt_i32 s23, 6
	s_cselect_b64 s[42:43], -1, 0
	s_cmp_gt_i32 s20, 5
	s_cselect_b64 s[44:45], -1, 0
	s_and_b64 s[42:43], s[42:43], s[44:45]
	s_cmp_lt_i32 s23, 7
	s_cselect_b64 s[44:45], -1, 0
	s_cmp_gt_i32 s20, 6
	s_cselect_b64 s[46:47], -1, 0
	s_and_b64 s[44:45], s[44:45], s[46:47]
	s_cmp_lt_i32 s23, 8
	s_cselect_b64 s[46:47], -1, 0
	s_cmp_gt_i32 s20, 7
	s_cselect_b64 s[48:49], -1, 0
	s_and_b64 s[46:47], s[46:47], s[48:49]
	s_cmp_lt_i32 s23, 9
	s_cselect_b64 s[48:49], -1, 0
	s_cmp_gt_i32 s20, 8
	s_cselect_b64 s[50:51], -1, 0
	s_and_b64 s[48:49], s[48:49], s[50:51]
	s_cmp_lt_i32 s23, 10
	s_cselect_b64 s[50:51], -1, 0
	s_cmp_gt_i32 s20, 9
	s_cselect_b64 s[52:53], -1, 0
	s_and_b64 s[50:51], s[50:51], s[52:53]
	s_cmp_lt_i32 s23, 11
	s_cselect_b64 s[52:53], -1, 0
	s_cmp_gt_i32 s20, 10
	s_cselect_b64 s[54:55], -1, 0
	s_and_b64 s[52:53], s[52:53], s[54:55]
	s_cmp_lt_i32 s23, 12
	s_cselect_b64 s[54:55], -1, 0
	s_cmp_gt_i32 s20, 11
	s_cselect_b64 s[56:57], -1, 0
	s_and_b64 s[54:55], s[54:55], s[56:57]
	s_cmp_lt_i32 s23, 13
	s_cselect_b64 s[56:57], -1, 0
	s_cmp_gt_i32 s20, 12
	s_cselect_b64 s[58:59], -1, 0
	s_and_b64 s[56:57], s[56:57], s[58:59]
	s_cmp_lt_i32 s23, 14
	s_cselect_b64 s[58:59], -1, 0
	s_cmp_gt_i32 s20, 13
	s_cselect_b64 s[60:61], -1, 0
	s_and_b64 s[58:59], s[58:59], s[60:61]
	s_cmp_lt_i32 s23, 15
	s_cselect_b64 s[60:61], -1, 0
	s_cmp_gt_i32 s20, 14
	s_cselect_b64 s[62:63], -1, 0
	s_and_b64 s[60:61], s[60:61], s[62:63]
	s_cmp_lt_i32 s23, 16
	s_movk_i32 s67, 0x940
	v_mul_u32_u24_e32 v2, 0x50, v2
	v_or_b32_e32 v4, s22, v1
	s_cselect_b64 s[22:23], -1, 0
	s_cmp_gt_i32 s20, 15
	v_mad_u32_u24 v2, v38, s67, v2
	s_cselect_b64 s[62:63], -1, 0
	v_and_or_b32 v5, v1, 60, v2
	v_lshlrev_b32_e32 v2, 2, v1
	s_and_b64 s[22:23], s[22:23], s[62:63]
	v_mul_lo_u32 v1, s20, v38
	s_movk_i32 s73, 0x110
	v_and_b32_e32 v0, 3, v0
	s_cmp_lg_u32 s20, 1
	v_mul_lo_u32 v7, v1, s73
	v_mul_u32_u24_e32 v0, 0x440, v0
	s_cselect_b64 s[62:63], -1, 0
	s_and_b32 s72, s20, 0x7ffffffe
	v_add3_u32 v23, v7, v0, s66
	v_add_u32_e32 v0, v6, v1
	s_bitcmp1_b32 s20, 0
	v_mul_lo_u32 v24, v0, s73
	s_mov_b32 s66, 0x8800
	v_mov_b32_e32 v0, 0xd040
	v_mul_u32_u24_e32 v3, 0x940, v38
	v_add_u32_e32 v20, 0x50, v5
	v_add_u32_e32 v21, 0xa0, v5
	v_add_u32_e32 v22, 0xf0, v5
	s_cselect_b64 s[64:65], -1, 0
	s_mul_i32 s74, s20, 0x660
	v_add3_u32 v25, v7, v2, s66
	v_mad_u32_u24 v26, v38, s67, v0
	s_mov_b64 s[66:67], 0
	s_mov_b32 s68, 0x3e000000
	s_mov_b32 s75, 0x3fb8aa3b
	s_mov_b32 s76, 0xc2ce8ed0
	s_mov_b32 s77, 0x42b17218
	s_mov_b32 s78, 0x43800000
	v_mov_b32_e32 v27, 0xff800000
	v_mov_b32_e32 v28, 0x7f800000
	s_branch .LBB0_7

.LBB0_59:
	s_endpgm
	s_endpgm
	s_endpgm
	s_endpgm
	s_endpgm
	s_endpgm
	s_endpgm
	s_endpgm
	s_endpgm
	s_endpgm
	s_endpgm
	s_endpgm
	s_endpgm
	s_endpgm
	s_endpgm
	s_endpgm
	s_endpgm
	s_endpgm
	s_endpgm
	s_endpgm
	s_endpgm
	s_endpgm
	s_endpgm
	s_endpgm
	s_endpgm
	s_endpgm
	s_endpgm
	s_endpgm
	s_endpgm
	s_endpgm
	.section	.rodata,"a",@progbits
	.p2align	6, 0x0

.LBB9_7:
	s_waitcnt vmcnt(0)
	s_load_dwordx4 s[0:3], s[0:1], 0x40
	s_ashr_i32 s4, s16, 31
	s_waitcnt vmcnt(1)
	v_lshlrev_b32_e32 v69, 5, v23
	v_lshl_or_b32 v70, s14, 7, v69
	v_mul_u32_u24_e32 v23, 0x2400, v23
	s_waitcnt lgkmcnt(0)
	s_mul_hi_u32 s8, s2, s16
	s_mul_i32 s4, s2, s4
	s_add_i32 s4, s8, s4
	s_mul_i32 s3, s3, s16
	s_add_i32 s3, s4, s3
	s_mul_i32 s2, s2, s16
	s_lshl_b64 s[2:3], s[2:3], 2
	s_add_u32 s4, s6, s2
	s_addc_u32 s6, s7, s3
	s_mul_hi_u32 s2, s0, s15
	s_mul_i32 s3, s0, s17
	s_add_i32 s2, s2, s3
	s_mul_i32 s3, s1, s15
	s_add_i32 s3, s2, s3
	s_mul_i32 s2, s0, s15
	s_lshl_b64 s[2:3], s[2:3], 2
	s_add_u32 s2, s4, s2
	s_addc_u32 s3, s6, s3
	v_ashrrev_i32_e32 v71, 31, v70
	v_lshlrev_b32_e32 v0, 4, v0
	v_accvgpr_read_b32 v68, a0
	v_accvgpr_read_b32 v67, a1
	v_lshl_add_u64 v[70:71], v[70:71], 2, s[2:3]
	v_and_b32_e32 v72, 0x70, v0
	v_mov_b32_e32 v73, 0
	v_lshl_or_b32 v22, v22, 2, v23
	s_movk_i32 s2, 0x240
	v_accvgpr_read_b32 v66, a2
	v_lshrrev_b32_e32 v69, 3, v1
	v_lshl_add_u64 v[0:1], v[70:71], 0, v[72:73]
	v_or_b32_e32 v70, v23, v72
	v_fma_f32 v23, s5, v68, 0
	v_mad_u32_u24 v68, v24, s2, v22
	v_fma_f32 v22, s5, v67, 0
	v_accvgpr_read_b32 v65, a3
	s_barrier
	ds_write_b32 v68, v22 offset:144
	v_fma_f32 v22, s5, v66, 0
	v_accvgpr_read_b32 v64, a4
	ds_write_b32 v68, v22 offset:288
	v_fma_f32 v22, s5, v65, 0
	v_accvgpr_read_b32 v63, a5
	ds_write_b32 v68, v22 offset:432
	v_fma_f32 v22, s5, v64, 0
	v_accvgpr_read_b32 v62, a6
	ds_write_b32 v68, v22 offset:1152
	v_fma_f32 v22, s5, v63, 0
	v_accvgpr_read_b32 v61, a7
	ds_write_b32 v68, v22 offset:1296
	v_fma_f32 v22, s5, v62, 0
	v_accvgpr_read_b32 v60, a8
	ds_write_b32 v68, v22 offset:1440
	v_fma_f32 v22, s5, v61, 0
	v_accvgpr_read_b32 v59, a9
	ds_write_b32 v68, v22 offset:1584
	v_fma_f32 v22, s5, v60, 0
	v_accvgpr_read_b32 v58, a10
	ds_write_b32 v68, v22 offset:2304
	v_fma_f32 v22, s5, v59, 0
	v_accvgpr_read_b32 v57, a11
	ds_write_b32 v68, v22 offset:2448
	v_fma_f32 v22, s5, v58, 0
	v_accvgpr_read_b32 v56, a12
	ds_write_b32 v68, v22 offset:2592
	v_fma_f32 v22, s5, v57, 0
	v_accvgpr_read_b32 v55, a13
	ds_write_b32 v68, v22 offset:2736
	v_fma_f32 v22, s5, v56, 0
	v_accvgpr_read_b32 v54, a14
	ds_write_b32 v68, v22 offset:3456
	v_fma_f32 v22, s5, v55, 0
	v_accvgpr_read_b32 v53, a15
	ds_write_b32 v68, v22 offset:3600
	v_fma_f32 v22, s5, v54, 0
	v_accvgpr_read_b32 v52, a16
	ds_write_b32 v68, v22 offset:3744
	v_fma_f32 v22, s5, v53, 0
	v_accvgpr_read_b32 v51, a17
	ds_write_b32 v68, v22 offset:3888
	v_fma_f32 v22, s5, v52, 0
	v_accvgpr_read_b32 v50, a18
	ds_write_b32 v68, v22 offset:4608
	v_fma_f32 v22, s5, v51, 0
	v_accvgpr_read_b32 v49, a19
	ds_write_b32 v68, v22 offset:4752
	v_fma_f32 v22, s5, v50, 0
	v_accvgpr_read_b32 v48, a20
	ds_write_b32 v68, v22 offset:4896
	v_fma_f32 v22, s5, v49, 0
	v_accvgpr_read_b32 v47, a21
	ds_write_b32 v68, v22 offset:5040
	v_fma_f32 v22, s5, v48, 0
	v_accvgpr_read_b32 v46, a22
	ds_write_b32 v68, v22 offset:5760
	v_fma_f32 v22, s5, v47, 0
	v_accvgpr_read_b32 v45, a23
	ds_write_b32 v68, v22 offset:5904
	v_fma_f32 v22, s5, v46, 0
	v_accvgpr_read_b32 v44, a24
	ds_write_b32 v68, v22 offset:6048
	v_fma_f32 v22, s5, v45, 0
	v_accvgpr_read_b32 v43, a25
	ds_write_b32 v68, v22 offset:6192
	v_fma_f32 v22, s5, v44, 0
	v_accvgpr_read_b32 v42, a26
	ds_write_b32 v68, v22 offset:6912
	v_fma_f32 v22, s5, v43, 0
	v_accvgpr_read_b32 v41, a27
	ds_write_b32 v68, v22 offset:7056
	v_fma_f32 v22, s5, v42, 0
	v_accvgpr_read_b32 v40, a28
	ds_write_b32 v68, v22 offset:7200
	v_fma_f32 v22, s5, v41, 0
	v_accvgpr_read_b32 v39, a29
	ds_write_b32 v68, v22 offset:7344
	v_fma_f32 v22, s5, v40, 0
	v_accvgpr_read_b32 v38, a30
	ds_write_b32 v68, v22 offset:8064
	v_fma_f32 v22, s5, v39, 0
	v_accvgpr_read_b32 v37, a31
	ds_write_b32 v68, v22 offset:8208
	v_fma_f32 v22, s5, v38, 0
	s_movk_i32 s4, 0x90
	ds_write_b32 v68, v22 offset:8352
	v_fma_f32 v22, s5, v37, 0
	v_mad_u32_u24 v71, v69, s4, v70
	ds_write_b32 v68, v23
	ds_write_b32 v68, v22 offset:8496
	ds_read_b128 v[104:107], v71
	ds_read_b128 v[108:111], v71 offset:1152
	ds_read_b128 v[112:115], v71 offset:2304
	ds_read_b128 v[116:119], v71 offset:3456
	ds_read_b128 v[120:123], v71 offset:4608
	ds_read_b128 v[124:127], v71 offset:5760
	ds_read_b128 v[128:131], v71 offset:6912
	ds_read_b128 v[132:135], v71 offset:8064
	v_mad_u64_u32 v[22:23], s[2:3], s0, v69, 0
	v_accvgpr_read_b32 v25, a43
	v_mov_b32_e32 v24, v23
	v_mad_u64_u32 v[42:43], s[2:3], s1, v69, v[24:25]
	v_mov_b32_e32 v23, v42
	v_or_b32_e32 v37, 8, v69
	v_lshl_add_u64 v[22:23], v[22:23], 2, v[0:1]
	v_mad_u32_u24 v46, v37, s4, v70
	s_waitcnt lgkmcnt(7)
	global_store_dwordx4 v[22:23], v[104:107], off sc1
	v_mad_u64_u32 v[22:23], s[2:3], s0, v37, 0
	v_mov_b32_e32 v24, v23
	v_mad_u64_u32 v[38:39], s[2:3], s1, v37, v[24:25]
	v_mov_b32_e32 v23, v38
	v_lshl_add_u64 v[22:23], v[22:23], 2, v[0:1]
	v_or_b32_e32 v37, 16, v69
	s_waitcnt lgkmcnt(6)
	global_store_dwordx4 v[22:23], v[108:111], off sc1
	v_mad_u64_u32 v[22:23], s[2:3], s0, v37, 0
	v_mov_b32_e32 v24, v23
	v_mad_u64_u32 v[42:43], s[2:3], s1, v37, v[24:25]
	v_mov_b32_e32 v23, v42
	v_lshl_add_u64 v[22:23], v[22:23], 2, v[0:1]
	v_or_b32_e32 v37, 24, v69
	s_waitcnt lgkmcnt(5)
	global_store_dwordx4 v[22:23], v[112:115], off sc1
	v_mad_u64_u32 v[22:23], s[2:3], s0, v37, 0
	v_mov_b32_e32 v24, v23
	v_mad_u64_u32 v[38:39], s[2:3], s1, v37, v[24:25]
	v_mov_b32_e32 v23, v38
	v_lshl_add_u64 v[22:23], v[22:23], 2, v[0:1]
	v_or_b32_e32 v37, 32, v69
	s_waitcnt lgkmcnt(4)
	global_store_dwordx4 v[22:23], v[116:119], off sc1
	v_mad_u64_u32 v[22:23], s[2:3], s0, v37, 0
	v_mov_b32_e32 v24, v23
	v_mad_u64_u32 v[42:43], s[2:3], s1, v37, v[24:25]
	v_mov_b32_e32 v23, v42
	v_lshl_add_u64 v[22:23], v[22:23], 2, v[0:1]
	v_or_b32_e32 v37, 40, v69
	s_waitcnt lgkmcnt(3)
	global_store_dwordx4 v[22:23], v[120:123], off sc1
	v_mad_u64_u32 v[22:23], s[2:3], s0, v37, 0
	v_mov_b32_e32 v24, v23
	v_mad_u64_u32 v[38:39], s[2:3], s1, v37, v[24:25]
	v_mov_b32_e32 v23, v38
	v_lshl_add_u64 v[22:23], v[22:23], 2, v[0:1]
	v_or_b32_e32 v37, 48, v69
	s_waitcnt lgkmcnt(2)
	global_store_dwordx4 v[22:23], v[124:127], off sc1
	v_mad_u64_u32 v[22:23], s[2:3], s0, v37, 0
	v_mov_b32_e32 v24, v23
	v_mad_u64_u32 v[42:43], s[2:3], s1, v37, v[24:25]
	v_mov_b32_e32 v23, v42
	v_lshl_add_u64 v[22:23], v[22:23], 2, v[0:1]
	v_or_b32_e32 v37, 56, v69
	s_waitcnt lgkmcnt(1)
	global_store_dwordx4 v[22:23], v[128:131], off sc1
	v_mad_u64_u32 v[22:23], s[2:3], s0, v37, 0
	v_mov_b32_e32 v24, v23
	v_mad_u64_u32 v[38:39], s[2:3], s1, v37, v[24:25]
	v_mov_b32_e32 v23, v38
	v_accvgpr_read_b32 v36, a32
	v_lshl_add_u64 v[22:23], v[22:23], 2, v[0:1]
	v_accvgpr_read_b32 v35, a33
	s_waitcnt lgkmcnt(0)
	global_store_dwordx4 v[22:23], v[132:135], off sc1
	v_fma_f32 v22, s5, v36, 0
	v_accvgpr_read_b32 v34, a34
	ds_write_b32 v68, v22
	v_fma_f32 v22, s5, v35, 0
	v_accvgpr_read_b32 v33, a35
	ds_write_b32 v68, v22 offset:144
	v_fma_f32 v22, s5, v34, 0
	v_accvgpr_read_b32 v32, a36
	ds_write_b32 v68, v22 offset:288
	v_fma_f32 v22, s5, v33, 0
	v_accvgpr_read_b32 v31, a37
	ds_write_b32 v68, v22 offset:432
	v_fma_f32 v22, s5, v32, 0
	v_accvgpr_read_b32 v30, a38
	ds_write_b32 v68, v22 offset:1152
	v_fma_f32 v22, s5, v31, 0
	v_accvgpr_read_b32 v29, a39
	ds_write_b32 v68, v22 offset:1296
	v_fma_f32 v22, s5, v30, 0
	v_accvgpr_read_b32 v28, a40
	ds_write_b32 v68, v22 offset:1440
	v_fma_f32 v22, s5, v29, 0
	v_accvgpr_read_b32 v27, a41
	ds_write_b32 v68, v22 offset:1584
	v_fma_f32 v22, s5, v28, 0
	v_accvgpr_read_b32 v26, a42
	ds_write_b32 v68, v22 offset:2304
	v_fma_f32 v22, s5, v27, 0
	v_accvgpr_read_b32 v17, a48
	v_accvgpr_read_b32 v16, a49
	v_accvgpr_read_b32 v15, a50
	v_accvgpr_read_b32 v14, a51
	v_accvgpr_read_b32 v13, a52
	v_accvgpr_read_b32 v12, a53
	v_accvgpr_read_b32 v11, a54
	v_accvgpr_read_b32 v10, a55
	v_accvgpr_read_b32 v9, a56
	v_accvgpr_read_b32 v8, a57
	v_accvgpr_read_b32 v7, a58
	v_accvgpr_read_b32 v6, a59
	v_accvgpr_read_b32 v5, a60
	v_accvgpr_read_b32 v4, a61
	v_accvgpr_read_b32 v3, a62
	v_accvgpr_read_b32 v2, a63
	v_accvgpr_read_b32 v21, a44
	v_accvgpr_read_b32 v20, a45
	v_accvgpr_read_b32 v19, a46
	v_accvgpr_read_b32 v18, a47
	ds_write_b32 v68, v22 offset:2448
	v_fma_f32 v22, s5, v26, 0
	ds_write_b32 v68, v22 offset:2592
	v_fma_f32 v22, s5, v25, 0
	v_fma_f32 v21, s5, v21, 0
	v_fma_f32 v20, s5, v20, 0
	v_fma_f32 v19, s5, v19, 0
	v_fma_f32 v18, s5, v18, 0
	v_fma_f32 v17, s5, v17, 0
	v_fma_f32 v16, s5, v16, 0
	v_fma_f32 v15, s5, v15, 0
	v_fma_f32 v14, s5, v14, 0
	v_fma_f32 v13, s5, v13, 0
	v_fma_f32 v12, s5, v12, 0
	v_fma_f32 v11, s5, v11, 0
	v_fma_f32 v10, s5, v10, 0
	v_fma_f32 v9, s5, v9, 0
	v_fma_f32 v8, s5, v8, 0
	v_fma_f32 v7, s5, v7, 0
	v_fma_f32 v6, s5, v6, 0
	v_fma_f32 v5, s5, v5, 0
	v_fma_f32 v4, s5, v4, 0
	v_fma_f32 v3, s5, v3, 0
	v_fma_f32 v2, s5, v2, 0
	ds_write_b32 v68, v22 offset:2736
	ds_write_b32 v68, v21 offset:3456
	ds_write_b32 v68, v20 offset:3600
	ds_write_b32 v68, v19 offset:3744
	ds_write_b32 v68, v18 offset:3888
	ds_write_b32 v68, v17 offset:4608
	ds_write_b32 v68, v16 offset:4752
	ds_write_b32 v68, v15 offset:4896
	ds_write_b32 v68, v14 offset:5040
	ds_write_b32 v68, v13 offset:5760
	ds_write_b32 v68, v12 offset:5904
	ds_write_b32 v68, v11 offset:6048
	ds_write_b32 v68, v10 offset:6192
	ds_write_b32 v68, v9 offset:6912
	ds_write_b32 v68, v8 offset:7056
	ds_write_b32 v68, v7 offset:7200
	ds_write_b32 v68, v6 offset:7344
	ds_write_b32 v68, v5 offset:8064
	ds_write_b32 v68, v4 offset:8208
	ds_write_b32 v68, v3 offset:8352
	ds_write_b32 v68, v2 offset:8496
	v_or_b32_e32 v9, 64, v69
	ds_read_b128 v[104:107], v71
	ds_read_b128 v[108:111], v71 offset:1152
	ds_read_b128 v[112:115], v71 offset:2304
	ds_read_b128 v[116:119], v71 offset:3456
	ds_read_b128 v[120:123], v71 offset:4608
	ds_read_b128 v[124:127], v71 offset:5760
	ds_read_b128 v[128:131], v71 offset:6912
	ds_read_b128 v[132:135], v71 offset:8064
	v_mad_u64_u32 v[6:7], s[2:3], s0, v9, 0
	v_mov_b32_e32 v8, v7
	v_mad_u64_u32 v[8:9], s[2:3], s1, v9, v[8:9]
	v_mov_b32_e32 v7, v8
	v_lshl_add_u64 v[10:11], v[6:7], 2, v[0:1]
	s_waitcnt lgkmcnt(7)
	global_store_dwordx4 v[10:11], v[104:107], off sc1
	s_nop 1
	v_or_b32_e32 v5, 0x48, v69
	v_mad_u64_u32 v[2:3], s[2:3], s0, v5, 0
	v_mov_b32_e32 v4, v3
	v_mad_u64_u32 v[4:5], s[2:3], s1, v5, v[4:5]
	v_mov_b32_e32 v3, v4
	v_lshl_add_u64 v[2:3], v[2:3], 2, v[0:1]
	s_waitcnt lgkmcnt(6)
	global_store_dwordx4 v[2:3], v[108:111], off sc1
	s_nop 0
	v_or_b32_e32 v9, 0x50, v69
	v_mad_u64_u32 v[6:7], s[2:3], s0, v9, 0
	v_mov_b32_e32 v8, v7
	v_mad_u64_u32 v[8:9], s[2:3], s1, v9, v[8:9]
	v_mov_b32_e32 v7, v8
	v_lshl_add_u64 v[10:11], v[6:7], 2, v[0:1]
	s_waitcnt lgkmcnt(5)
	global_store_dwordx4 v[10:11], v[112:115], off sc1
	s_nop 1
	v_or_b32_e32 v5, 0x58, v69
	v_mad_u64_u32 v[2:3], s[2:3], s0, v5, 0
	v_mov_b32_e32 v4, v3
	v_mad_u64_u32 v[4:5], s[2:3], s1, v5, v[4:5]
	v_mov_b32_e32 v3, v4
	v_lshl_add_u64 v[2:3], v[2:3], 2, v[0:1]
	s_waitcnt lgkmcnt(4)
	global_store_dwordx4 v[2:3], v[116:119], off sc1
	s_nop 0
	v_or_b32_e32 v9, 0x60, v69
	v_mad_u64_u32 v[6:7], s[2:3], s0, v9, 0
	v_mov_b32_e32 v8, v7
	v_mad_u64_u32 v[8:9], s[2:3], s1, v9, v[8:9]
	v_mov_b32_e32 v7, v8
	v_lshl_add_u64 v[10:11], v[6:7], 2, v[0:1]
	s_waitcnt lgkmcnt(3)
	global_store_dwordx4 v[10:11], v[120:123], off sc1
	s_nop 1
	v_or_b32_e32 v5, 0x68, v69
	v_mad_u64_u32 v[2:3], s[2:3], s0, v5, 0
	v_mov_b32_e32 v4, v3
	v_mad_u64_u32 v[4:5], s[2:3], s1, v5, v[4:5]
	v_mov_b32_e32 v3, v4
	v_lshl_add_u64 v[2:3], v[2:3], 2, v[0:1]
	s_waitcnt lgkmcnt(2)
	global_store_dwordx4 v[2:3], v[124:127], off sc1
	s_nop 0
	v_or_b32_e32 v9, 0x70, v69
	v_mad_u64_u32 v[6:7], s[2:3], s0, v9, 0
	v_mov_b32_e32 v8, v7
	v_mad_u64_u32 v[8:9], s[2:3], s1, v9, v[8:9]
	v_mov_b32_e32 v7, v8
	v_lshl_add_u64 v[10:11], v[6:7], 2, v[0:1]
	s_waitcnt lgkmcnt(1)
	global_store_dwordx4 v[10:11], v[128:131], off sc1
	s_nop 1
	v_or_b32_e32 v5, 0x78, v69
	v_mad_u64_u32 v[2:3], s[2:3], s0, v5, 0
	v_mov_b32_e32 v4, v3
	v_mad_u64_u32 v[4:5], s[0:1], s1, v5, v[4:5]
	v_mov_b32_e32 v3, v4
	v_lshl_add_u64 v[0:1], v[2:3], 2, v[0:1]
	s_waitcnt lgkmcnt(0)
	global_store_dwordx4 v[0:1], v[132:135], off sc1
	s_endpgm
	s_endpgm
	s_endpgm
	s_endpgm
	s_endpgm
	s_endpgm
	s_endpgm
	s_endpgm
	s_endpgm
	s_endpgm
	s_endpgm
	s_endpgm
	s_endpgm
	s_endpgm
	s_endpgm
	s_endpgm
	s_endpgm
	s_endpgm
	s_endpgm
	s_endpgm
	s_endpgm
	s_endpgm
	s_endpgm
	s_endpgm
	s_endpgm
	s_endpgm
	s_endpgm
	s_endpgm
	s_endpgm
	s_endpgm
	s_endpgm
	s_endpgm
	s_endpgm
	s_endpgm
	s_endpgm
	s_endpgm
	s_endpgm
	s_endpgm
	s_endpgm
	s_endpgm
	s_endpgm
	s_endpgm
	s_endpgm
	s_endpgm
	s_endpgm
	s_endpgm
	s_endpgm
	s_endpgm
	s_endpgm
	s_endpgm
	s_endpgm
	s_endpgm
	s_endpgm
	s_endpgm
	s_endpgm
	s_endpgm
	s_endpgm
	s_endpgm
	s_endpgm
	s_endpgm
	s_endpgm

.LBB10_7:
	s_waitcnt vmcnt(0)
	s_load_dwordx4 s[0:3], s[0:1], 0x40
	s_ashr_i32 s4, s16, 31
	s_waitcnt vmcnt(7)
	v_lshlrev_b32_e32 v37, 5, v11
	v_lshl_or_b32 v38, s14, 7, v37
	v_mul_u32_u24_e32 v37, 0x2400, v11
	s_waitcnt lgkmcnt(0)
	s_mul_hi_u32 s8, s2, s16
	s_mul_i32 s4, s2, s4
	s_add_i32 s4, s8, s4
	s_mul_i32 s3, s3, s16
	s_add_i32 s3, s4, s3
	s_mul_hi_u32 s4, s0, s15
	s_mul_i32 s8, s0, s17
	s_add_i32 s4, s4, s8
	s_mul_i32 s8, s1, s15
	v_accvgpr_read_b32 v36, a0
	s_waitcnt vmcnt(2)
	v_accvgpr_read_b32 v35, a1
	s_add_i32 s9, s4, s8
	v_lshl_or_b32 v10, v10, 2, v37
	s_movk_i32 s4, 0x240
	v_accvgpr_read_b32 v34, a2
	v_accvgpr_read_b32 v33, a3
	v_fma_f32 v36, s5, v36, 0
	v_mad_u32_u24 v10, v12, s4, v10
	v_fma_f32 v12, s5, v35, 0
	v_accvgpr_read_b32 v32, a4
	v_accvgpr_read_b32 v31, a5
	s_barrier
	ds_write2_b32 v10, v36, v12 offset1:36
	v_fma_f32 v12, s5, v34, 0
	v_fma_f32 v33, s5, v33, 0
	v_accvgpr_read_b32 v30, a6
	v_accvgpr_read_b32 v29, a7
	ds_write2_b32 v10, v12, v33 offset0:72 offset1:108
	v_fma_f32 v12, s5, v32, 0
	v_fma_f32 v31, s5, v31, 0
	v_add_u32_e32 v32, 0x400, v10
	v_accvgpr_read_b32 v28, a8
	v_accvgpr_read_b32 v27, a9
	ds_write2_b32 v32, v12, v31 offset0:32 offset1:68
	v_fma_f32 v12, s5, v30, 0
	v_fma_f32 v29, s5, v29, 0
	v_accvgpr_read_b32 v26, a10
	v_accvgpr_read_b32 v25, a11
	ds_write2_b32 v32, v12, v29 offset0:104 offset1:140
	v_fma_f32 v12, s5, v28, 0
	v_fma_f32 v27, s5, v27, 0
	v_add_u32_e32 v28, 0x800, v10
	v_accvgpr_read_b32 v24, a12
	v_accvgpr_read_b32 v23, a13
	ds_write2_b32 v28, v12, v27 offset0:64 offset1:100
	v_fma_f32 v12, s5, v26, 0
	v_fma_f32 v25, s5, v25, 0
	v_accvgpr_read_b32 v22, a14
	v_accvgpr_read_b32 v21, a15
	ds_write2_b32 v28, v12, v25 offset0:136 offset1:172
	v_fma_f32 v12, s5, v24, 0
	v_fma_f32 v23, s5, v23, 0
	v_add_u32_e32 v24, 0xc00, v10
	v_accvgpr_read_b32 v20, a16
	v_accvgpr_read_b32 v19, a17
	ds_write2_b32 v24, v12, v23 offset0:96 offset1:132
	v_fma_f32 v12, s5, v22, 0
	v_fma_f32 v21, s5, v21, 0
	v_accvgpr_read_b32 v18, a18
	v_accvgpr_read_b32 v17, a19
	ds_write2_b32 v24, v12, v21 offset0:168 offset1:204
	v_fma_f32 v12, s5, v20, 0
	v_fma_f32 v19, s5, v19, 0
	v_add_u32_e32 v20, 0x1000, v10
	v_accvgpr_read_b32 v16, a20
	v_accvgpr_read_b32 v15, a21
	ds_write2_b32 v20, v12, v19 offset0:128 offset1:164
	v_fma_f32 v12, s5, v18, 0
	v_fma_f32 v17, s5, v17, 0
	v_accvgpr_read_b32 v14, a22
	v_accvgpr_read_b32 v13, a23
	s_mul_i32 s2, s2, s16
	ds_write2_b32 v20, v12, v17 offset0:200 offset1:236
	v_fma_f32 v12, s5, v16, 0
	v_fma_f32 v15, s5, v15, 0
	v_add_u32_e32 v16, 0x1400, v10
	v_accvgpr_read_b32 v9, a24
	v_accvgpr_read_b32 v8, a25
	ds_write2_b32 v16, v12, v15 offset0:160 offset1:196
	v_fma_f32 v12, s5, v14, 0
	v_fma_f32 v13, s5, v13, 0
	v_add_u32_e32 v14, 0x1600, v10
	s_lshl_b64 s[2:3], s[2:3], 2
	v_accvgpr_read_b32 v7, a26
	v_accvgpr_read_b32 v6, a27
	v_accvgpr_read_b32 v5, a28
	v_accvgpr_read_b32 v4, a29
	v_accvgpr_read_b32 v3, a30
	v_accvgpr_read_b32 v2, a31
	s_mul_i32 s8, s0, s15
	ds_write2_b32 v14, v12, v13 offset0:104 offset1:140
	v_fma_f32 v9, s5, v9, 0
	v_fma_f32 v8, s5, v8, 0
	v_add_u32_e32 v12, 0x1800, v10
	s_add_u32 s4, s6, s2
	ds_write2_b32 v12, v9, v8 offset0:192 offset1:228
	v_fma_f32 v7, s5, v7, 0
	v_fma_f32 v6, s5, v6, 0
	v_add_u32_e32 v8, 0x1c00, v10
	v_fma_f32 v5, s5, v5, 0
	v_fma_f32 v4, s5, v4, 0
	v_fma_f32 v3, s5, v3, 0
	v_fma_f32 v2, s5, v2, 0
	s_addc_u32 s5, s7, s3
	s_lshl_b64 s[2:3], s[8:9], 2
	ds_write2_b32 v8, v7, v6 offset0:8 offset1:44
	v_add_u32_e32 v6, 0x1e00, v10
	s_add_u32 s2, s4, s2
	v_lshlrev_b32_e32 v0, 4, v0
	v_ashrrev_i32_e32 v39, 31, v38
	ds_write2_b32 v6, v5, v4 offset0:96 offset1:132
	v_add_u32_e32 v4, 0x2000, v10
	s_addc_u32 s3, s5, s3
	v_and_b32_e32 v10, 0x70, v0
	ds_write2_b32 v4, v3, v2 offset0:40 offset1:76
	v_lshrrev_b32_e32 v12, 3, v1
	v_lshl_add_u64 v[2:3], v[38:39], 2, s[2:3]
	v_or_b32_e32 v0, v37, v10
	s_movk_i32 s2, 0x90
	v_mov_b32_e32 v11, 0
	v_mad_u32_u24 v13, v12, s2, v0
	v_lshl_add_u64 v[8:9], v[2:3], 0, v[10:11]
	ds_read_b128 v[56:59], v13
	ds_read_b128 v[60:63], v13 offset:1152
	ds_read_b128 v[64:67], v13 offset:2304
	ds_read_b128 v[68:71], v13 offset:3456
	ds_read_b128 v[72:75], v13 offset:4608
	ds_read_b128 v[76:79], v13 offset:5760
	ds_read_b128 v[80:83], v13 offset:6912
	ds_read_b128 v[84:87], v13 offset:8064
	v_mad_u64_u32 v[4:5], s[2:3], s0, v12, 0
	v_mov_b32_e32 v6, v5
	v_mad_u64_u32 v[6:7], s[2:3], s1, v12, v[6:7]
	v_mov_b32_e32 v5, v6
	v_lshl_add_u64 v[10:11], v[4:5], 2, v[8:9]
	s_waitcnt lgkmcnt(7)
	global_store_dwordx4 v[10:11], v[56:59], off sc1
	s_nop 1
	v_or_b32_e32 v3, 8, v12
	v_mad_u64_u32 v[0:1], s[2:3], s0, v3, 0
	v_mov_b32_e32 v2, v1
	v_mad_u64_u32 v[2:3], s[2:3], s1, v3, v[2:3]
	v_mov_b32_e32 v1, v2
	v_lshl_add_u64 v[0:1], v[0:1], 2, v[8:9]
	s_waitcnt lgkmcnt(6)
	global_store_dwordx4 v[0:1], v[60:63], off sc1
	s_nop 0
	v_or_b32_e32 v7, 16, v12
	v_mad_u64_u32 v[4:5], s[2:3], s0, v7, 0
	v_mov_b32_e32 v6, v5
	v_mad_u64_u32 v[6:7], s[2:3], s1, v7, v[6:7]
	v_mov_b32_e32 v5, v6
	v_lshl_add_u64 v[10:11], v[4:5], 2, v[8:9]
	s_waitcnt lgkmcnt(5)
	global_store_dwordx4 v[10:11], v[64:67], off sc1
	s_nop 1
	v_or_b32_e32 v3, 24, v12
	v_mad_u64_u32 v[0:1], s[2:3], s0, v3, 0
	v_mov_b32_e32 v2, v1
	v_mad_u64_u32 v[2:3], s[2:3], s1, v3, v[2:3]
	v_mov_b32_e32 v1, v2
	v_lshl_add_u64 v[0:1], v[0:1], 2, v[8:9]
	s_waitcnt lgkmcnt(4)
	global_store_dwordx4 v[0:1], v[68:71], off sc1
	s_nop 0
	v_or_b32_e32 v7, 32, v12
	v_mad_u64_u32 v[4:5], s[2:3], s0, v7, 0
	v_mov_b32_e32 v6, v5
	v_mad_u64_u32 v[6:7], s[2:3], s1, v7, v[6:7]
	v_mov_b32_e32 v5, v6
	v_lshl_add_u64 v[10:11], v[4:5], 2, v[8:9]
	s_waitcnt lgkmcnt(3)
	global_store_dwordx4 v[10:11], v[72:75], off sc1
	s_nop 1
	v_or_b32_e32 v3, 40, v12
	v_mad_u64_u32 v[0:1], s[2:3], s0, v3, 0
	v_mov_b32_e32 v2, v1
	v_mad_u64_u32 v[2:3], s[2:3], s1, v3, v[2:3]
	v_mov_b32_e32 v1, v2
	v_lshl_add_u64 v[0:1], v[0:1], 2, v[8:9]
	s_waitcnt lgkmcnt(2)
	global_store_dwordx4 v[0:1], v[76:79], off sc1
	s_nop 0
	v_or_b32_e32 v7, 48, v12
	v_mad_u64_u32 v[4:5], s[2:3], s0, v7, 0
	v_mov_b32_e32 v6, v5
	v_mad_u64_u32 v[6:7], s[2:3], s1, v7, v[6:7]
	v_mov_b32_e32 v5, v6
	v_lshl_add_u64 v[10:11], v[4:5], 2, v[8:9]
	s_waitcnt lgkmcnt(1)
	global_store_dwordx4 v[10:11], v[80:83], off sc1
	s_nop 1
	v_or_b32_e32 v3, 56, v12
	v_mad_u64_u32 v[0:1], s[2:3], s0, v3, 0
	v_mov_b32_e32 v2, v1
	v_mad_u64_u32 v[2:3], s[0:1], s1, v3, v[2:3]
	v_mov_b32_e32 v1, v2
	v_lshl_add_u64 v[0:1], v[0:1], 2, v[8:9]
	s_waitcnt lgkmcnt(0)
	global_store_dwordx4 v[0:1], v[84:87], off sc1
	s_endpgm
	s_endpgm
	s_endpgm
	s_endpgm
	s_endpgm
	s_endpgm
	s_endpgm
	s_endpgm
	s_endpgm
	s_endpgm
	s_endpgm
	s_endpgm
	s_endpgm
	s_endpgm
	s_endpgm
	s_endpgm
	s_endpgm
	s_endpgm
	s_endpgm
	s_endpgm
	s_endpgm
	s_endpgm
	s_endpgm
	s_endpgm
	s_endpgm
	s_endpgm
	s_endpgm
	s_endpgm
	s_endpgm
	s_endpgm
	s_endpgm
	s_endpgm
	s_endpgm
	s_endpgm
	s_endpgm
	s_endpgm
